# v60 + static s_setprio 1 for waves 4-7 from the conv phase on (until the next GEMM's reset)
# speedup vs baseline: 1.0106x; 1.0018x over previous
; #define LAS __attribute__((address_space(3)))
; __device__ __forceinline__ int lt_tid(int wv) { int ln; asm volatile("v_mbcnt_lo_u32_b32 %0, -1, 0\n\tv_mbcnt_hi_u32_b32 %0, -1, %0" : "=v"(ln)); return (wv << 6) | ln; }
; __device__ __forceinline__ void ph_conv2(const Params& p, int l, LAS unsigned char* lds, const int wvid) {
;     ...
;     const int tid = lt_tid(wvid), c = tid & 255, th = tid >> 8;
;     const bf16_t* U = (const bf16_t*)(ws + WS_U); bf16_t* MIX = (bf16_t*)(ws + WS_MIX);
;     LAS float* G = (LAS float*)lds;
;     const float* cw = p.in[I_CONVW] + (size_t)l * 31 * 256; const float cb = p.in[I_CONVB][l * 256 + c], gg = p.in[I_GNG][l * 256 + c], gb = p.in[I_GNB][l * 256 + c];
;     float wv[31];
; #pragma unroll
;     for (int w = 0; w < 31; ++w) wv[w] = cw[w * 256 + c];
;     const bool bal = (int)gridDim.x == 256;
;     const int nkk = bal ? 3 : (NB * 64 + (int)gridDim.x - 1) / (int)gridDim.x;
;     for (int kk = 0; kk < nkk; ++kk) {
;         int unit;
;         if (!bal) unit = bid + kk * (int)gridDim.x;
;         else if (kk < 2) unit = (bid >= 32 && bid < 40) ? NB * 64 : bid + 256 * kk;
;         else unit = (bid >= 40 && bid < 56) ? (bid < 48 ? bid - 8 : bid + 240) : NB * 64;
;         if (unit >= NB * 64) continue;
;         const int b = unit >> 6, t0 = (unit & 63) * 64, ntok = (unit & 63) == 63 ? 80 : 64, nrow = ntok + 30;
;         __syncthreads();
;         { u32x4 av[7], gv[7];
; #pragma unroll
;           for (int q = 0; q < 7; ++q) { const int it = tid + q * NTHR, row = it >> 5, ch = it & 31, tt = t0 - 30 + row;
;               const bf16_t* ur = U + ((size_t)b * LT + min(max(tt, 0), LT - 1)) * INW; av[q] = *(const u32x4*)(ur + C_CA + ch * 8); gv[q] = *(const u32x4*)(ur + C_CG + ch * 8);
.LBB0_438:
	s_cmp_lt_i32 s11, 1
	s_cbranch_scc1 .LBB0_478
	v_lshlrev_b32_e32 v0, 3, v3
	v_or_b32_e32 v6, s75, v3
	v_and_b32_e32 v54, 0xf8, v0
	v_lshlrev_b32_e32 v0, 1, v2
	s_add_u32 s0, s6, 0x4090000
	v_lshl_add_u64 v[4:5], s[6:7], 0, v[0:1]
	v_add_u32_e32 v0, 0x200, v6
	s_addc_u32 s1, s7, 0
	s_sub_i32 s4, s10, 40
	v_ashrrev_i32_e32 v93, 5, v0
	v_add_u32_e32 v0, 0x400, v6
	s_cmp_lt_i32 s10, 48
	v_ashrrev_i32_e32 v94, 5, v0
	v_add_u32_e32 v0, 0x600, v6
	s_cselect_b32 s5, -8, 0xf0
	v_ashrrev_i32_e32 v95, 5, v0
	v_add_u32_e32 v0, 0x800, v6
	s_add_i32 s5, s5, s10
	v_ashrrev_i32_e32 v96, 5, v0
	v_add_u32_e32 v0, 0xa00, v6
	s_cmp_lt_u32 s4, 16
	v_ashrrev_i32_e32 v97, 5, v0
	v_add_u32_e32 v0, 0xc00, v6
	s_cselect_b32 s16, s5, 0x200
	s_and_b32 s4, s10, -8
	s_mov_b64 s[6:7], 0xf1f0600
	v_ashrrev_i32_e32 v92, 5, v6
	v_ashrrev_i32_e32 v98, 5, v0
	v_ashrrev_i32_e32 v91, 8, v6
	s_cmp_eq_u32 s4, 32
	v_lshl_add_u32 v3, v54, 2, 0
	v_lshl_add_u64 v[56:57], v[4:5], 0, s[6:7]
	v_lshlrev_b32_e32 v0, 10, v92
	v_lshlrev_b32_e32 v4, 10, v93
	v_lshlrev_b32_e32 v5, 10, v94
	v_lshlrev_b32_e32 v6, 10, v95
	v_lshlrev_b32_e32 v7, 10, v96
	v_lshlrev_b32_e32 v8, 10, v97
	v_lshlrev_b32_e32 v9, 10, v98
	s_cselect_b64 s[4:5], -1, 0
	v_lshl_add_u32 v99, v2, 2, 0
	s_mov_b32 s17, 0
	v_add_u32_e32 v100, v3, v0
	v_add_u32_e32 v101, v3, v4
	v_add_u32_e32 v102, v3, v5
	v_add_u32_e32 v103, v3, v6
	v_add_u32_e32 v104, v3, v7
	v_add_u32_e32 v105, v3, v8
	v_add_u32_e32 v106, v3, v9
	s_cmp_lt_u32 s74, 0x100
	s_cbranch_scc1 .Lcvprio
	s_setprio 1
